# burst loads use offset:N immediates (8 VMEM + 4 SALU per 8KiB burst instead of 8 + 16); otherwise the ring-16 hybrid with last-chunk early flush
# speedup vs baseline: 1.0341x; 1.0049x over previous
.Lk1_scan:
	s_load_dwordx2 s[4:5], s[0:1], 0x0
	s_load_dwordx4 s[8:11], s[0:1], 0x20
	s_load_dwordx2 s[12:13], s[0:1], 0x30
	v_and_b32_e32 v6, 63, v0
	v_readfirstlane_b32 s3, v0
	v_lshlrev_b32_e32 v1, 4, v6
	v_lshlrev_b32_e32 v2, 2, v6
	v_or_b32_e32 v3, 1, v2
	v_or_b32_e32 v4, 2, v2
	v_or_b32_e32 v5, 3, v2
	s_lshr_b32 s3, s3, 6
	s_sub_u32 s16, s2, 0x60
	s_lshl_b32 s16, s16, 2
	s_add_u32 s16, s16, s3
	s_mul_i32 s17, s16, 0x48000
	s_lshr_b32 s18, s17, 2
	s_lshl_b32 s24, s3, 13
	s_mov_b32 s25, s24
	s_mov_b32 s28, s24
	s_mov_b32 s36, 0
	s_mov_b64 s[62:63], 0
	v_mov_b32_e32 v21, 1
	s_mov_b32 s27, 0
	s_mov_b32 s29, 0x55555556
	s_mov_b32 s31, 0xc0000
	s_waitcnt lgkmcnt(0)
	s_and_b32 s50, s16, 15
	s_mul_i32 s52, s50, 512
	s_add_u32 s52, s52, 28672
	s_lshl_b32 s53, s50, 6
	s_add_u32 s53, s53, 0xe000
	s_add_u32 s54, s10, s53
	s_addc_u32 s55, s11, 0
	s_mul_i32 s59, s16, 14
	s_mul_i32 s57, s59, 0x4000
	s_lshr_b32 s18, s57, 2
	s_add_u32 s6, s4, s57
	s_addc_u32 s7, s5, 0
	v_mov_b32_e32 v27, 0
	global_load_dwordx4 v[28:31], v1, s[6:7] nt
	global_load_dwordx4 v[32:35], v1, s[6:7] offset:1024 nt
	global_load_dwordx4 v[36:39], v1, s[6:7] offset:2048 nt
	global_load_dwordx4 v[40:43], v1, s[6:7] offset:3072 nt
	s_add_u32 s6, s6, 0x1000
	s_addc_u32 s7, s7, 0
	global_load_dwordx4 v[44:47], v1, s[6:7] nt
	global_load_dwordx4 v[48:51], v1, s[6:7] offset:1024 nt
	global_load_dwordx4 v[52:55], v1, s[6:7] offset:2048 nt
	global_load_dwordx4 v[56:59], v1, s[6:7] offset:3072 nt
	s_add_u32 s6, s6, 0x1000
	s_addc_u32 s7, s7, 0
	global_load_dwordx4 v[60:63], v1, s[6:7] nt
	global_load_dwordx4 v[64:67], v1, s[6:7] offset:1024 nt
	global_load_dwordx4 v[68:71], v1, s[6:7] offset:2048 nt
	global_load_dwordx4 v[72:75], v1, s[6:7] offset:3072 nt
	s_add_u32 s6, s6, 0x1000
	s_addc_u32 s7, s7, 0
	global_load_dwordx4 v[76:79], v1, s[6:7] nt
	global_load_dwordx4 v[80:83], v1, s[6:7] offset:1024 nt
	global_load_dwordx4 v[84:87], v1, s[6:7] offset:2048 nt
	global_load_dwordx4 v[88:91], v1, s[6:7] offset:3072 nt
	s_add_u32 s6, s6, 0x1000
	s_addc_u32 s7, s7, 0
	s_mov_b32 s26, 18
	s_add_u32 s57, s59, 1
	s_mul_i32 s57, s57, 0x4000
	s_lshr_b32 s58, s57, 2
	s_add_u32 s6, s4, s57
	s_addc_u32 s7, s5, 0
	s_mov_b32 s26, 0

.Lk1_contm_7:
	global_load_dwordx4 v[28:31], v1, s[6:7] nt
	global_load_dwordx4 v[32:35], v1, s[6:7] offset:1024 nt
	global_load_dwordx4 v[36:39], v1, s[6:7] offset:2048 nt
	global_load_dwordx4 v[40:43], v1, s[6:7] offset:3072 nt
	s_add_u32 s6, s6, 0x1000
	s_addc_u32 s7, s7, 0
	global_load_dwordx4 v[44:47], v1, s[6:7] nt
	global_load_dwordx4 v[48:51], v1, s[6:7] offset:1024 nt
	global_load_dwordx4 v[52:55], v1, s[6:7] offset:2048 nt
	global_load_dwordx4 v[56:59], v1, s[6:7] offset:3072 nt
	s_add_u32 s6, s6, 0x1000
	s_addc_u32 s7, s7, 0
	s_waitcnt vmcnt(15)
	v_or3_b32 v12, v60, v61, v62
	v_or_b32_e32 v12, v12, v63
	v_cmp_ne_u32_e32 vcc, 0, v12
	s_cbranch_vccnz .Lk1_hitm_8

.Lk1_contm_15:
	global_load_dwordx4 v[60:63], v1, s[6:7] nt
	global_load_dwordx4 v[64:67], v1, s[6:7] offset:1024 nt
	global_load_dwordx4 v[68:71], v1, s[6:7] offset:2048 nt
	global_load_dwordx4 v[72:75], v1, s[6:7] offset:3072 nt
	s_add_u32 s6, s6, 0x1000
	s_addc_u32 s7, s7, 0
	global_load_dwordx4 v[76:79], v1, s[6:7] nt
	global_load_dwordx4 v[80:83], v1, s[6:7] offset:1024 nt
	global_load_dwordx4 v[84:87], v1, s[6:7] offset:2048 nt
	global_load_dwordx4 v[88:91], v1, s[6:7] offset:3072 nt
	s_add_u32 s6, s6, 0x1000
	s_addc_u32 s7, s7, 0
	s_mov_b32 s18, s58
	s_add_u32 s60, s26, 2
	s_cmp_lt_u32 s60, 14
	s_cbranch_scc0 .Lk1_dynid
	s_add_u32 s57, s59, s60
	s_branch .Lk1_haveid
